# P3c: loop-invariant gamma loads issued once before the row loop; P6c tail: the 14 late LN2 gamma/beta loads issued with the first pair, per-store load-wait chain removed
# speedup vs baseline: 1.0478x; 1.0073x over previous
; __device__ __forceinline__ unsigned pk2(float lo, float hi) { return pkbf(lo, hi); }
; __device__ __forceinline__ void row_mixnorm(const Params& P, unsigned char* ws, int l, int rowi, int lane) {
;     const u2* yp = (const u2*)((const bf16*)(ws + WS_YMIX) + (size_t)rowi * D) + lane; const f4* ysg = (const f4*)((const float*)(ws + WS_YSG) + (size_t)rowi * 512) + lane;
;     const f4* gp = (const f4*)(P.in[14] + (size_t)l * D) + lane;
;     f4 v[8]; float ss[8];
; #pragma unroll
;     for (int j = 0; j < 8; ++j) { if (j == 2 || j == 3) v[j] = ysg[64 * (j - 2)]; else { const u2 w = yp[64 * j]; v[j] = mk_f4(__uint_as_float(w.x << 16), __uint_as_float(w.x & 0xffff0000u), __uint_as_float(w.y << 16), __uint_as_float(w.y & 0xffff0000u));
;             if (j >= 4) { const u2 w1 = yp[64 * j + YB_SEL / 4], w2 = yp[64 * j + YB_WIN / 4];
;                 v[j] += mk_f4(__uint_as_float(w1.x << 16), __uint_as_float(w1.x & 0xffff0000u), __uint_as_float(w1.y << 16), __uint_as_float(w1.y & 0xffff0000u)) + mk_f4(__uint_as_float(w2.x << 16), __uint_as_float(w2.x & 0xffff0000u), __uint_as_float(w2.y << 16), __uint_as_float(w2.y & 0xffff0000u)); } }
;         ss[j] = v[j].x * v[j].x + v[j].y * v[j].y + v[j].z * v[j].z + v[j].w * v[j].w; }
;     const float r0 = rsqrtf(wave_sum(ss[0] + ss[1]) * (1.f / 512.f) + LN_EPS);
;     const float r1 = rsqrtf(wave_sum(ss[2] + ss[3]) * (1.f / 512.f) + LN_EPS);
;     const float r2 = rsqrtf(wave_sum((ss[4] + ss[5]) + (ss[6] + ss[7])) * (1.f / 1024.f) + LN_EPS);
;     u2* op = (u2*)((bf16*)(ws + WS_MIXED) + (size_t)rowi * D) + lane;
; #pragma unroll
;     for (int j = 0; j < 8; ++j) { const float r = (j < 2) ? r0 : ((j < 4) ? r1 : r2); const f4 g4 = gp[64 * j];
;         op[64 * j] = mk_u2(pk2(v[j].x * r * g4.x, v[j].y * r * g4.y), pk2(v[j].z * r * g4.z, v[j].w * r * g4.w)); }
.LBB0_570:
	s_andn2_b64 vcc, exec, s[4:5]
	s_cbranch_vccnz .LBB0_630
	v_mbcnt_lo_u32_b32 v0, -1, 0
	v_mbcnt_hi_u32_b32 v0, -1, v0
	s_mov_b32 s12, 0x3a800000
	v_or_b32_e32 v1, s91, v0
	v_readlane_b32 s14, v254, 50
	v_readfirstlane_b32 s4, v1
	s_ashr_i32 s4, s4, 6
	s_add_i32 s8, s4, s87
	s_mov_b64 s[6:7], s[92:93]
	s_cmpk_lt_i32 s8, 0x2000
	s_mov_b32 s13, 0x3b000000
	v_readlane_b32 s15, v254, 51
	s_cbranch_scc0 .LBB0_574
	v_readlane_b32 s10, v254, 52
	v_readlane_b32 s11, v254, 53
	s_lshl_b32 s5, s10, 13
	v_readlane_b32 s10, v254, 4
	v_and_b32_e32 v2, 63, v0
	v_readlane_b32 s11, v254, 5
	s_add_u32 s10, s10, s5
	s_addc_u32 s11, s11, 0
	v_lshlrev_b32_e32 v0, 4, v2
	v_mov_b32_e32 v1, v80
	v_lshl_add_u64 v[12:13], s[10:11], 0, v[0:1]
	v_and_b32_e32 v1, 64, v226
	v_add_u32_e32 v1, 64, v1
	v_xor_b32_e32 v3, 1, v226
	v_cmp_lt_i32_e32 vcc, v3, v1
	s_mov_b64 s[10:11], 0x1000
	v_lshl_add_u64 v[14:15], v[12:13], 0, s[10:11]
	v_cndmask_b32_e32 v3, v226, v3, vcc
	v_lshlrev_b32_e32 v43, 2, v3
	v_xor_b32_e32 v3, 2, v226
	v_cmp_lt_i32_e32 vcc, v3, v1
	s_mov_b64 s[10:11], 0x1400
	s_ashr_i32 s5, s4, 31
	v_cndmask_b32_e32 v3, v226, v3, vcc
	v_lshlrev_b32_e32 v45, 2, v3
	v_xor_b32_e32 v3, 4, v226
	v_cmp_lt_i32_e32 vcc, v3, v1
	s_waitcnt vmcnt(11)
	v_lshl_add_u64 v[16:17], v[12:13], 0, s[10:11]
	s_mov_b64 s[10:11], 0x1800
	v_cndmask_b32_e32 v3, v226, v3, vcc
	v_lshlrev_b32_e32 v53, 2, v3
	v_xor_b32_e32 v3, 8, v226
	s_add_u32 s4, s87, s4
	v_readlane_b32 s9, v253, 41
	v_lshl_add_u64 v[18:19], v[12:13], 0, s[10:11]
	s_mov_b64 s[10:11], 0x1c00
	v_cmp_lt_i32_e32 vcc, v3, v1
	s_addc_u32 s5, s9, s5
	s_waitcnt vmcnt(10)
	v_lshl_add_u64 v[20:21], v[12:13], 0, s[10:11]
	v_cndmask_b32_e32 v1, v226, v3, vcc
	s_lshl_b64 s[10:11], s[4:5], 12
	s_lshl_b64 s[4:5], s[4:5], 11
	v_lshlrev_b32_e32 v54, 2, v1
	v_lshl_or_b32 v22, v2, 3, s10
	v_mov_b32_e32 v23, s11
	s_waitcnt vmcnt(9)
	v_or_b32_e32 v24, s4, v0
	v_mov_b32_e32 v25, s5
	global_load_dwordx4 v[100:103], v[12:13], off
	global_load_dwordx4 v[104:107], v[12:13], off offset:1024
	global_load_dwordx4 v[108:111], v[12:13], off offset:2048
	global_load_dwordx4 v[112:115], v[12:13], off offset:3072
	global_load_dwordx4 v[116:119], v[14:15], off
	global_load_dwordx4 v[120:123], v[16:17], off
	global_load_dwordx4 v[124:127], v[18:19], off
	global_load_dwordx4 v[128:131], v[20:21], off
.LBB0_573:
	v_lshl_add_u64 v[8:9], s[6:7], 0, v[22:23]
	v_add_co_u32_e32 v26, vcc, 0x2f400000, v8
	v_lshl_add_u64 v[0:1], s[6:7], 0, v[24:25]
	s_nop 0
	v_addc_co_u32_e32 v27, vcc, 0, v9, vcc
	v_add_co_u32_e32 v0, vcc, 0x45400000, v0
	global_load_dwordx2 v[46:47], v[26:27], off
	global_load_dwordx2 v[10:11], v[26:27], off offset:512
	v_addc_co_u32_e32 v1, vcc, 0, v1, vcc
	s_waitcnt vmcnt(10)
	v_add_co_u32_e32 v28, vcc, 0x31400000, v8
	global_load_dwordx4 v[4:7], v[0:1], off
	s_nop 0
	global_load_dwordx4 v[0:3], v[0:1], off offset:1024
	s_nop 0
	global_load_dwordx2 v[30:31], v[26:27], off offset:2048
	v_addc_co_u32_e32 v29, vcc, 0, v9, vcc
	v_add_co_u32_e32 v34, vcc, 0x43400000, v8
	global_load_dwordx2 v[32:33], v[28:29], off offset:2048
	s_nop 0
	v_addc_co_u32_e32 v35, vcc, 0, v9, vcc
	s_waitcnt lgkmcnt(0)
	global_load_dwordx2 v[36:37], v[34:35], off offset:2048
	global_load_dwordx2 v[48:49], v[26:27], off offset:2560
	global_load_dwordx2 v[50:51], v[28:29], off offset:2560
	global_load_dwordx2 v[56:57], v[34:35], off offset:2560
	global_load_dwordx2 v[58:59], v[26:27], off offset:3072
	global_load_dwordx2 v[60:61], v[28:29], off offset:3072
	global_load_dwordx2 v[62:63], v[34:35], off offset:3072
	s_nop 0
	global_load_dwordx2 v[28:29], v[28:29], off offset:3584
	s_add_i32 s8, s8, s74
	global_load_dwordx2 v[34:35], v[34:35], off offset:3584
	v_lshl_add_u64 v[22:23], v[22:23], 0, s[14:15]
	global_load_dwordx2 v[26:27], v[26:27], off offset:3584
	v_lshl_add_u64 v[24:25], v[24:25], 0, s[28:29]
	s_cmpk_gt_i32 s8, 0x1fff
	s_waitcnt vmcnt(15)
	v_lshlrev_b32_e32 v64, 16, v46
	v_and_b32_e32 v65, 0xffff0000, v46
	s_waitcnt vmcnt(2)
	v_lshlrev_b32_e32 v38, 16, v28
	v_and_b32_e32 v39, 0xffff0000, v28
	v_lshlrev_b32_e32 v28, 16, v29
	v_and_b32_e32 v29, 0xffff0000, v29
	s_waitcnt vmcnt(1)
	v_lshlrev_b32_e32 v40, 16, v34
	v_and_b32_e32 v41, 0xffff0000, v34
	v_lshlrev_b32_e32 v34, 16, v35
	v_and_b32_e32 v35, 0xffff0000, v35
	v_pk_add_f32 v[38:39], v[38:39], v[40:41]
	v_pk_add_f32 v[28:29], v[28:29], v[34:35]
	s_waitcnt vmcnt(0)
; __device__ __forceinline__ void row_mixnorm(const Params& P, unsigned char* ws, int l, int rowi, int lane) {
;     const u2* yp = (const u2*)((const bf16*)(ws + WS_YMIX) + (size_t)rowi * D) + lane; const f4* ysg = (const f4*)((const float*)(ws + WS_YSG) + (size_t)rowi * 512) + lane;
;     const f4* gp = (const f4*)(P.in[14] + (size_t)l * D) + lane;
;     f4 v[8]; float ss[8];
; #pragma unroll
;     for (int j = 0; j < 8; ++j) { if (j == 2 || j == 3) v[j] = ysg[64 * (j - 2)]; else { const u2 w = yp[64 * j]; v[j] = mk_f4(__uint_as_float(w.x << 16), __uint_as_float(w.x & 0xffff0000u), __uint_as_float(w.y << 16), __uint_as_float(w.y & 0xffff0000u));
;             if (j >= 4) { const u2 w1 = yp[64 * j + YB_SEL / 4], w2 = yp[64 * j + YB_WIN / 4];
;                 v[j] += mk_f4(__uint_as_float(w1.x << 16), __uint_as_float(w1.x & 0xffff0000u), __uint_as_float(w1.y << 16), __uint_as_float(w1.y & 0xffff0000u)) + mk_f4(__uint_as_float(w2.x << 16), __uint_as_float(w2.x & 0xffff0000u), __uint_as_float(w2.y << 16), __uint_as_float(w2.y & 0xffff0000u)); } }
;         ss[j] = v[j].x * v[j].x + v[j].y * v[j].y + v[j].z * v[j].z + v[j].w * v[j].w; }
;     const float r0 = rsqrtf(wave_sum(ss[0] + ss[1]) * (1.f / 512.f) + LN_EPS);
;     const float r1 = rsqrtf(wave_sum(ss[2] + ss[3]) * (1.f / 512.f) + LN_EPS);
;     const float r2 = rsqrtf(wave_sum((ss[4] + ss[5]) + (ss[6] + ss[7])) * (1.f / 1024.f) + LN_EPS);
	v_lshlrev_b32_e32 v34, 16, v26
	v_and_b32_e32 v35, 0xffff0000, v26
	v_lshlrev_b32_e32 v26, 16, v27
	v_and_b32_e32 v27, 0xffff0000, v27
	v_pk_add_f32 v[26:27], v[28:29], v[26:27]
	v_pk_add_f32 v[28:29], v[38:39], v[34:35]
	v_lshlrev_b32_e32 v34, 16, v32
	v_and_b32_e32 v35, 0xffff0000, v32
	v_lshlrev_b32_e32 v32, 16, v33
	v_and_b32_e32 v33, 0xffff0000, v33
	v_lshlrev_b32_e32 v38, 16, v36
	v_and_b32_e32 v39, 0xffff0000, v36
	v_lshlrev_b32_e32 v36, 16, v37
	v_and_b32_e32 v37, 0xffff0000, v37
	v_pk_add_f32 v[32:33], v[32:33], v[36:37]
	v_pk_add_f32 v[34:35], v[34:35], v[38:39]
	v_lshlrev_b32_e32 v36, 16, v30
	v_and_b32_e32 v37, 0xffff0000, v30
	v_lshlrev_b32_e32 v30, 16, v31
	v_and_b32_e32 v31, 0xffff0000, v31
	v_pk_add_f32 v[40:41], v[34:35], v[36:37]
	v_pk_add_f32 v[38:39], v[32:33], v[30:31]
	v_lshlrev_b32_e32 v30, 16, v50
	v_and_b32_e32 v31, 0xffff0000, v50
	v_lshlrev_b32_e32 v32, 16, v51
	v_and_b32_e32 v33, 0xffff0000, v51
	v_lshlrev_b32_e32 v34, 16, v56
	v_and_b32_e32 v35, 0xffff0000, v56
	v_lshlrev_b32_e32 v36, 16, v57
	v_and_b32_e32 v37, 0xffff0000, v57
	v_pk_add_f32 v[32:33], v[32:33], v[36:37]
	v_pk_add_f32 v[30:31], v[30:31], v[34:35]
	v_lshlrev_b32_e32 v34, 16, v48
	v_and_b32_e32 v35, 0xffff0000, v48
	v_lshlrev_b32_e32 v48, 16, v49
	v_and_b32_e32 v49, 0xffff0000, v49
	v_pk_add_f32 v[36:37], v[30:31], v[34:35]
	v_pk_add_f32 v[34:35], v[32:33], v[48:49]
	v_lshlrev_b32_e32 v30, 16, v60
	v_and_b32_e32 v31, 0xffff0000, v60
	v_lshlrev_b32_e32 v32, 16, v61
	v_and_b32_e32 v33, 0xffff0000, v61
	v_lshlrev_b32_e32 v48, 16, v62
	v_and_b32_e32 v49, 0xffff0000, v62
	v_lshlrev_b32_e32 v50, 16, v63
	v_and_b32_e32 v51, 0xffff0000, v63
	v_pk_add_f32 v[50:51], v[32:33], v[50:51]
	v_pk_add_f32 v[30:31], v[30:31], v[48:49]
	v_lshlrev_b32_e32 v32, 16, v58
	v_and_b32_e32 v33, 0xffff0000, v58
	v_lshlrev_b32_e32 v48, 16, v59
	v_and_b32_e32 v49, 0xffff0000, v59
	v_pk_add_f32 v[32:33], v[30:31], v[32:33]
	v_pk_add_f32 v[30:31], v[50:51], v[48:49]
	v_mul_f32_e32 v42, v33, v33
	v_mul_f32_e32 v44, v37, v37
	v_mul_f32_e32 v48, v41, v41
	v_mul_f32_e32 v52, v29, v29
	v_fmac_f32_e32 v42, v32, v32
	v_fmac_f32_e32 v44, v36, v36
	v_fmac_f32_e32 v48, v40, v40
	v_mul_f32_e32 v49, v1, v1
	v_mul_f32_e32 v50, v5, v5
	v_fmac_f32_e32 v52, v28, v28
	v_fmac_f32_e32 v42, v30, v30
	v_fmac_f32_e32 v44, v34, v34
	v_fmac_f32_e32 v48, v38, v38
	v_fmac_f32_e32 v49, v0, v0
	v_fmac_f32_e32 v50, v4, v4
	v_fmac_f32_e32 v52, v26, v26
	v_fmac_f32_e32 v42, v31, v31
	v_fmac_f32_e32 v44, v35, v35
	v_fmac_f32_e32 v48, v39, v39
	v_fmac_f32_e32 v49, v2, v2
	v_fmac_f32_e32 v50, v6, v6
	v_fmac_f32_e32 v52, v27, v27
	v_fmac_f32_e32 v49, v3, v3
	v_fmac_f32_e32 v50, v7, v7
	v_add_f32_e32 v44, v48, v44
	v_add_f32_e32 v42, v42, v52
	v_add_f32_e32 v49, v50, v49
	v_add_f32_e32 v42, v44, v42
	ds_bpermute_b32 v50, v43, v49
	ds_bpermute_b32 v44, v43, v42
	v_mov_b64_e32 v[56:57], v[100:101]
	v_mov_b64_e32 v[58:59], v[102:103]
	v_lshlrev_b32_e32 v60, 16, v47
	v_and_b32_e32 v61, 0xffff0000, v47
	s_waitcnt lgkmcnt(1)
	v_add_f32_e32 v49, v49, v50
	s_waitcnt lgkmcnt(0)
	v_add_f32_e32 v42, v42, v44
	ds_bpermute_b32 v50, v45, v49
	ds_bpermute_b32 v44, v45, v42
	v_pk_mul_f32 v[46:47], v[64:65], v[64:65]
	v_pk_mul_f32 v[62:63], v[60:61], v[60:61]
	s_waitcnt lgkmcnt(1)
	v_add_f32_e32 v49, v49, v50
	s_waitcnt lgkmcnt(0)
	v_add_f32_e32 v42, v42, v44
	ds_bpermute_b32 v50, v53, v49
	ds_bpermute_b32 v44, v53, v42
	s_waitcnt lgkmcnt(1)
	v_add_f32_e32 v49, v49, v50
	s_waitcnt lgkmcnt(0)
	v_add_f32_e32 v42, v42, v44
	ds_bpermute_b32 v50, v54, v49
	ds_bpermute_b32 v44, v54, v42
	s_waitcnt lgkmcnt(1)
	v_add_f32_e32 v49, v49, v50
	s_waitcnt lgkmcnt(0)
	v_add_f32_e32 v42, v42, v44
	v_mov_b32_e32 v50, v49
	v_mov_b32_e32 v44, v42
	s_nop 0
	v_permlane16_swap_b32_e32 v49, v50
	v_permlane16_swap_b32_e32 v42, v44
	v_add_f32_e32 v49, v49, v50
	v_add_f32_e32 v48, v42, v44
	v_mov_b32_e32 v51, v49
	v_mov_b32_e32 v50, v48
	s_nop 0
	v_permlane32_swap_b32_e32 v49, v51
	v_permlane32_swap_b32_e32 v48, v50
	v_pk_add_f32 v[48:49], v[48:49], v[50:51]
	v_lshlrev_b32_e32 v50, 16, v10
	v_pk_fma_f32 v[48:49], v[48:49], s[12:13], v[194:195] op_sel_hi:[1,1,0]
	v_and_b32_e32 v51, 0xffff0000, v10
	v_mul_f32_e32 v42, 0x4b800000, v49
	v_cmp_gt_f32_e64 s[4:5], s57, v49
	v_cmp_gt_f32_e32 vcc, s57, v48
	s_nop 0
	v_cndmask_b32_e64 v42, v49, v42, s[4:5]
	v_rsq_f32_e32 v42, v42
	v_and_b32_e32 v49, 0xffff0000, v11
	v_mul_f32_e32 v44, 0x45800000, v42
	v_cndmask_b32_e64 v44, v42, v44, s[4:5]
	v_mul_f32_e32 v42, 0x4b800000, v48
	v_cndmask_b32_e32 v42, v48, v42, vcc
	v_rsq_f32_e32 v42, v42
	s_mov_b32 s4, 0x33400000
	v_pk_mul_f32 v[4:5], v[4:5], v[44:45] op_sel_hi:[1,0]
	v_pk_mul_f32 v[6:7], v[6:7], v[44:45] op_sel_hi:[1,0]
	v_mul_f32_e32 v48, 0x45800000, v42
	v_cndmask_b32_e32 v42, v42, v48, vcc
	v_lshlrev_b32_e32 v48, 16, v11
	v_pk_mul_f32 v[10:11], v[50:51], v[50:51]
	v_pk_mul_f32 v[66:67], v[48:49], v[48:49]
	v_add_f32_e32 v10, v10, v11
	v_add_f32_e32 v11, v46, v47
	v_add_f32_e32 v10, v66, v10
	v_add_f32_e32 v11, v62, v11
	v_add_f32_e32 v10, v67, v10
	v_add_f32_e32 v11, v63, v11
	v_add_f32_e32 v10, v11, v10
	ds_bpermute_b32 v11, v43, v10
	v_pk_mul_f32 v[0:1], v[0:1], v[44:45] op_sel_hi:[1,0]
	v_pk_mul_f32 v[2:3], v[2:3], v[44:45] op_sel_hi:[1,0]
	s_waitcnt lgkmcnt(0)
; __device__ __forceinline__ unsigned pk2(float lo, float hi) { return pkbf(lo, hi); }
; __device__ __forceinline__ void row_mixnorm(const Params& P, unsigned char* ws, int l, int rowi, int lane) {
;     ...
;     const float r0 = rsqrtf(wave_sum(ss[0] + ss[1]) * (1.f / 512.f) + LN_EPS);
;     const float r1 = rsqrtf(wave_sum(ss[2] + ss[3]) * (1.f / 512.f) + LN_EPS);
;     const float r2 = rsqrtf(wave_sum((ss[4] + ss[5]) + (ss[6] + ss[7])) * (1.f / 1024.f) + LN_EPS);
;     u2* op = (u2*)((bf16*)(ws + WS_MIXED) + (size_t)rowi * D) + lane;
; #pragma unroll
;     for (int j = 0; j < 8; ++j) { const float r = (j < 2) ? r0 : ((j < 4) ? r1 : r2); const f4 g4 = gp[64 * j];
;         op[64 * j] = mk_u2(pk2(v[j].x * r * g4.x, v[j].y * r * g4.y), pk2(v[j].z * r * g4.z, v[j].w * r * g4.w)); }
	v_add_f32_e32 v10, v10, v11
	ds_bpermute_b32 v11, v45, v10
	s_waitcnt lgkmcnt(0)
	v_add_f32_e32 v10, v10, v11
	ds_bpermute_b32 v11, v53, v10
	s_waitcnt lgkmcnt(0)
	v_add_f32_e32 v10, v10, v11
	ds_bpermute_b32 v11, v54, v10
	s_waitcnt lgkmcnt(0)
	v_add_f32_e32 v10, v10, v11
	v_mov_b32_e32 v11, v10
	s_nop 1
	v_permlane16_swap_b32_e32 v10, v11
	v_add_f32_e32 v10, v10, v11
	v_mov_b32_e32 v11, v10
	s_nop 1
	v_permlane32_swap_b32_e32 v10, v11
	v_add_f32_e32 v10, v10, v11
	v_fmamk_f32 v10, v10, 0x3b000000, v194
	v_cmp_gt_f32_e32 vcc, s57, v10
	v_mul_f32_e32 v11, 0x4b800000, v10
	s_nop 0
	v_cndmask_b32_e32 v10, v10, v11, vcc
	v_rsq_f32_e32 v10, v10
	s_nop 0
	v_mul_f32_e32 v11, 0x45800000, v10
	v_cndmask_b32_e32 v52, v10, v11, vcc
	v_pk_mul_f32 v[10:11], v[52:53], v[64:65] op_sel_hi:[0,1]
	v_pk_mul_f32 v[46:47], v[52:53], v[60:61] op_sel_hi:[0,1]
	s_nop 0
	v_pk_mul_f32 v[10:11], v[10:11], v[56:57]
	v_pk_mul_f32 v[46:47], v[46:47], v[58:59]
	v_cvt_pk_bf16_f32 v10, v10, v11
	v_cvt_pk_bf16_f32 v11, v46, v47
	v_add_co_u32_e32 v46, vcc, s4, v8
	v_pk_mul_f32 v[50:51], v[52:53], v[50:51] op_sel_hi:[0,1]
	s_nop 0
	v_addc_co_u32_e32 v47, vcc, 0, v9, vcc
	global_store_dwordx2 v[46:47], v[10:11], off
	v_mov_b64_e32 v[8:9], v[104:105]
	v_mov_b64_e32 v[10:11], v[106:107]
	v_pk_mul_f32 v[48:49], v[52:53], v[48:49] op_sel_hi:[0,1]
	s_nop 0
	v_pk_mul_f32 v[8:9], v[50:51], v[8:9]
	v_pk_mul_f32 v[10:11], v[48:49], v[10:11]
	v_cvt_pk_bf16_f32 v8, v8, v9
	v_cvt_pk_bf16_f32 v9, v10, v11
	global_store_dwordx2 v[46:47], v[8:9], off offset:512
	v_mov_b64_e32 v[8:9], v[108:109]
	v_mov_b64_e32 v[10:11], v[110:111]
	s_nop 0
	v_pk_mul_f32 v[4:5], v[4:5], v[8:9]
	v_pk_mul_f32 v[6:7], v[6:7], v[10:11]
	v_cvt_pk_bf16_f32 v4, v4, v5
	v_cvt_pk_bf16_f32 v5, v6, v7
	global_store_dwordx2 v[46:47], v[4:5], off offset:1024
	v_mov_b64_e32 v[4:5], v[112:113]
	v_mov_b64_e32 v[6:7], v[114:115]
	s_nop 0
	v_pk_mul_f32 v[0:1], v[0:1], v[4:5]
	v_pk_mul_f32 v[2:3], v[2:3], v[6:7]
	v_cvt_pk_bf16_f32 v0, v0, v1
	v_cvt_pk_bf16_f32 v1, v2, v3
	global_store_dwordx2 v[46:47], v[0:1], off offset:1536
	v_mov_b64_e32 v[0:1], v[116:117]
	v_mov_b64_e32 v[2:3], v[118:119]
	v_pk_mul_f32 v[4:5], v[40:41], v[42:43] op_sel_hi:[1,0]
	s_nop 0
	v_pk_mul_f32 v[0:1], v[0:1], v[4:5]
	v_pk_mul_f32 v[4:5], v[38:39], v[42:43] op_sel_hi:[1,0]
	v_cvt_pk_bf16_f32 v0, v0, v1
	v_pk_mul_f32 v[2:3], v[2:3], v[4:5]
	v_pk_mul_f32 v[4:5], v[36:37], v[42:43] op_sel_hi:[1,0]
	v_cvt_pk_bf16_f32 v1, v2, v3
	global_store_dwordx2 v[46:47], v[0:1], off offset:2048
	v_mov_b64_e32 v[0:1], v[120:121]
	v_mov_b64_e32 v[2:3], v[122:123]
	s_nop 0
	v_pk_mul_f32 v[0:1], v[4:5], v[0:1]
	v_pk_mul_f32 v[4:5], v[34:35], v[42:43] op_sel_hi:[1,0]
	v_cvt_pk_bf16_f32 v0, v0, v1
	v_pk_mul_f32 v[2:3], v[4:5], v[2:3]
	v_pk_mul_f32 v[4:5], v[32:33], v[42:43] op_sel_hi:[1,0]
	v_cvt_pk_bf16_f32 v1, v2, v3
	global_store_dwordx2 v[46:47], v[0:1], off offset:2560
	v_mov_b64_e32 v[0:1], v[124:125]
	v_mov_b64_e32 v[2:3], v[126:127]
	s_nop 0
	v_pk_mul_f32 v[0:1], v[4:5], v[0:1]
	v_pk_mul_f32 v[4:5], v[30:31], v[42:43] op_sel_hi:[1,0]
	v_cvt_pk_bf16_f32 v0, v0, v1
	v_pk_mul_f32 v[2:3], v[4:5], v[2:3]
	v_pk_mul_f32 v[4:5], v[28:29], v[42:43] op_sel_hi:[1,0]
	v_cvt_pk_bf16_f32 v1, v2, v3
	global_store_dwordx2 v[46:47], v[0:1], off offset:3072
	v_mov_b64_e32 v[0:1], v[128:129]
	v_mov_b64_e32 v[2:3], v[130:131]
	s_nop 0
	v_pk_mul_f32 v[0:1], v[4:5], v[0:1]
	v_pk_mul_f32 v[4:5], v[26:27], v[42:43] op_sel_hi:[1,0]
	v_cvt_pk_bf16_f32 v0, v0, v1
	v_pk_mul_f32 v[2:3], v[4:5], v[2:3]
	s_nop 0
	v_cvt_pk_bf16_f32 v1, v2, v3
	global_store_dwordx2 v[46:47], v[0:1], off offset:3584
	s_cbranch_scc0 .LBB0_573

; __device__ __forceinline__ void row_peer_reduce(const Params& P, unsigned char* ws, int l, int rowi, int lane, float* __restrict__ xout) {
;     ...
; #pragma unroll 4
;     for (int xb_ = 0; xb_ < 8; ++xb_) { const u4 a = *(const u4*)(PARTQ + ((size_t)xb_ * NTOK + ((n + 5u * (unsigned)xb_) & (size_t)(NTOK - 1))) * 1024u + (unsigned)(16 * lane)); const float psc = PSCL[(size_t)xb_ * NTOK + n];
; #pragma unroll
;         for (int d = 0; d < 4; ++d) { const f2 p0 = __builtin_amdgcn_cvt_scalef32_pk_f32_fp4(a[d], 1.0f, 0), p1 = __builtin_amdgcn_cvt_scalef32_pk_f32_fp4(a[d], 1.0f, 1), p2 = __builtin_amdgcn_cvt_scalef32_pk_f32_fp4(a[d], 1.0f, 2), p3 = __builtin_amdgcn_cvt_scalef32_pk_f32_fp4(a[d], 1.0f, 3);
;             const int o = 16 * (d >> 1) + 8 * (d & 1);
;             acc[o] += psc * p0.x; acc[o + 1] += psc * p0.y; acc[o + 2] += psc * p1.x; acc[o + 3] += psc * p1.y; acc[o + 4] += psc * p2.x; acc[o + 5] += psc * p2.y; acc[o + 6] += psc * p3.x; acc[o + 7] += psc * p3.y; } }
.Lp6c_join:
	s_and_b32 s22, s50, 0x1fff
	s_add_u32 s26, s4, s22
	s_addc_u32 s27, s5, 0
	s_and_b32 s22, s49, 0x1fff
	s_add_u32 s28, s14, s22
	s_addc_u32 s29, s15, 0
	s_and_b32 s22, s48, 0x1fff
	s_add_u32 s30, s16, s22
	s_addc_u32 s31, s17, 0
	s_and_b32 s22, s47, 0x1fff
	s_add_u32 s22, s18, s22
	s_addc_u32 s23, s19, 0
	s_lshl_b64 s[22:23], s[22:23], 10
	s_add_u32 s22, s41, s34
	v_mov_b64_e32 v[6:7], v[156:157]
	v_mov_b64_e32 v[8:9], v[158:159]
	s_addc_u32 s23, s42, s35
	v_mov_b32_e32 v10, v172
	s_lshl_b64 s[30:31], s[30:31], 10
	s_lshl_b64 s[28:29], s[28:29], 10
	s_lshl_b64 s[26:27], s[26:27], 10
	s_add_u32 s34, s34, 0x20000
	s_addc_u32 s35, s35, 0
	s_add_u32 s4, s4, 0x8000
	s_addc_u32 s5, s5, 0
	s_add_i32 s50, s50, 20
	s_add_u32 s14, s14, 0x8000
	s_addc_u32 s15, s15, 0
	s_add_i32 s49, s49, 20
	s_add_u32 s16, s16, 0x8000
	s_addc_u32 s17, s17, 0
	s_add_i32 s48, s48, 20
	s_add_u32 s18, s18, 0x8000
	s_addc_u32 s19, s19, 0
	s_add_i32 s47, s47, 20
	s_cmp_eq_u32 s34, 0x40000
	s_nop 0
	v_cvt_scalef32_pk_f32_fp4 v[18:19], v6, 1.0 op_sel:[0,1,0]
	v_cvt_scalef32_pk_f32_fp4 v[24:25], v6, 1.0 op_sel:[1,1,0]
	s_nop 0
	v_pk_fma_f32 v[18:19], v[10:11], v[18:19], v[60:61] op_sel_hi:[0,1,1]
	v_pk_fma_f32 v[24:25], v[10:11], v[24:25], v[62:63] op_sel_hi:[0,1,1]
	v_cvt_scalef32_pk_f32_fp4 v[26:27], v7, 1.0
	v_cvt_scalef32_pk_f32_fp4 v[60:61], v8, 1.0 op_sel:[1,0,0]
	v_cvt_scalef32_pk_f32_fp4 v[62:63], v8, 1.0 op_sel:[0,1,0]
	v_cvt_scalef32_pk_f32_fp4 v[14:15], v6, 1.0
	v_cvt_scalef32_pk_f32_fp4 v[16:17], v6, 1.0 op_sel:[1,0,0]
	v_pk_fma_f32 v[26:27], v[10:11], v[26:27], v[64:65] op_sel_hi:[0,1,1]
	v_cvt_scalef32_pk_f32_fp4 v[64:65], v8, 1.0 op_sel:[1,1,0]
	v_pk_fma_f32 v[28:29], v[10:11], v[60:61], v[28:29] op_sel_hi:[0,1,1]
	v_pk_fma_f32 v[20:21], v[10:11], v[62:63], v[20:21] op_sel_hi:[0,1,1]
	v_cvt_scalef32_pk_f32_fp4 v[60:61], v9, 1.0
	v_cvt_scalef32_pk_f32_fp4 v[62:63], v9, 1.0 op_sel:[1,0,0]
	v_pk_fma_f32 v[14:15], v[10:11], v[14:15], v[56:57] op_sel_hi:[0,1,1]
	v_pk_fma_f32 v[16:17], v[10:11], v[16:17], v[58:59] op_sel_hi:[0,1,1]
	v_cvt_scalef32_pk_f32_fp4 v[30:31], v7, 1.0 op_sel:[1,0,0]
	v_cvt_scalef32_pk_f32_fp4 v[56:57], v7, 1.0 op_sel:[0,1,0]
	v_cvt_scalef32_pk_f32_fp4 v[6:7], v7, 1.0 op_sel:[1,1,0]
	v_cvt_scalef32_pk_f32_fp4 v[58:59], v8, 1.0
	v_pk_fma_f32 v[22:23], v[10:11], v[64:65], v[22:23] op_sel_hi:[0,1,1]
	v_cvt_scalef32_pk_f32_fp4 v[64:65], v9, 1.0 op_sel:[0,1,0]
	v_cvt_scalef32_pk_f32_fp4 v[8:9], v9, 1.0 op_sel:[1,1,0]
	v_pk_fma_f32 v[12:13], v[10:11], v[60:61], v[12:13] op_sel_hi:[0,1,1]
	v_pk_fma_f32 v[60:61], v[10:11], v[62:63], v[0:1] op_sel_hi:[0,1,1]
	v_pk_fma_f32 v[30:31], v[10:11], v[30:31], v[66:67] op_sel_hi:[0,1,1]
	v_pk_fma_f32 v[56:57], v[10:11], v[56:57], v[68:69] op_sel_hi:[0,1,1]
	v_pk_fma_f32 v[6:7], v[10:11], v[6:7], v[70:71] op_sel_hi:[0,1,1]
	v_pk_fma_f32 v[58:59], v[10:11], v[58:59], v[72:73] op_sel_hi:[0,1,1]
	v_pk_fma_f32 v[4:5], v[10:11], v[64:65], v[4:5] op_sel_hi:[0,1,1]
	v_pk_fma_f32 v[8:9], v[10:11], v[8:9], v[2:3] op_sel_hi:[0,1,1]
	v_mov_b64_e32 v[0:1], v[160:161]
	v_mov_b64_e32 v[2:3], v[162:163]
	s_nop 0
	v_mov_b32_e32 v10, v173
	s_nop 0
	v_cvt_scalef32_pk_f32_fp4 v[62:63], v0, 1.0
	v_cvt_scalef32_pk_f32_fp4 v[64:65], v0, 1.0 op_sel:[1,0,0]
	v_cvt_scalef32_pk_f32_fp4 v[66:67], v0, 1.0 op_sel:[0,1,0]
	v_cvt_scalef32_pk_f32_fp4 v[68:69], v0, 1.0 op_sel:[1,1,0]
	s_nop 0
	v_pk_fma_f32 v[14:15], v[10:11], v[62:63], v[14:15] op_sel_hi:[0,1,1]
	v_pk_fma_f32 v[16:17], v[10:11], v[64:65], v[16:17] op_sel_hi:[0,1,1]
	v_pk_fma_f32 v[18:19], v[10:11], v[66:67], v[18:19] op_sel_hi:[0,1,1]
	v_cvt_scalef32_pk_f32_fp4 v[62:63], v1, 1.0
	v_cvt_scalef32_pk_f32_fp4 v[64:65], v1, 1.0 op_sel:[1,0,0]
	v_cvt_scalef32_pk_f32_fp4 v[66:67], v1, 1.0 op_sel:[0,1,0]
	v_cvt_scalef32_pk_f32_fp4 v[0:1], v1, 1.0 op_sel:[1,1,0]
	v_pk_fma_f32 v[6:7], v[10:11], v[0:1], v[6:7] op_sel_hi:[0,1,1]
	v_cvt_scalef32_pk_f32_fp4 v[0:1], v2, 1.0
	v_pk_fma_f32 v[26:27], v[10:11], v[62:63], v[26:27] op_sel_hi:[0,1,1]
	v_pk_fma_f32 v[30:31], v[10:11], v[64:65], v[30:31] op_sel_hi:[0,1,1]
	v_cvt_scalef32_pk_f32_fp4 v[62:63], v2, 1.0 op_sel:[1,0,0]
	v_cvt_scalef32_pk_f32_fp4 v[64:65], v2, 1.0 op_sel:[0,1,0]
	v_pk_fma_f32 v[58:59], v[10:11], v[0:1], v[58:59] op_sel_hi:[0,1,1]
	v_cvt_scalef32_pk_f32_fp4 v[0:1], v3, 1.0
	v_pk_fma_f32 v[56:57], v[10:11], v[66:67], v[56:57] op_sel_hi:[0,1,1]
	v_cvt_scalef32_pk_f32_fp4 v[66:67], v2, 1.0 op_sel:[1,1,0]
	v_pk_fma_f32 v[28:29], v[10:11], v[62:63], v[28:29] op_sel_hi:[0,1,1]
	v_pk_fma_f32 v[20:21], v[10:11], v[64:65], v[20:21] op_sel_hi:[0,1,1]
	v_cvt_scalef32_pk_f32_fp4 v[62:63], v3, 1.0 op_sel:[1,0,0]
	v_cvt_scalef32_pk_f32_fp4 v[64:65], v3, 1.0 op_sel:[0,1,0]
	v_cvt_scalef32_pk_f32_fp4 v[2:3], v3, 1.0 op_sel:[1,1,0]
	v_pk_fma_f32 v[12:13], v[10:11], v[0:1], v[12:13] op_sel_hi:[0,1,1]
	v_pk_fma_f32 v[24:25], v[10:11], v[68:69], v[24:25] op_sel_hi:[0,1,1]
	v_pk_fma_f32 v[22:23], v[10:11], v[66:67], v[22:23] op_sel_hi:[0,1,1]
	v_pk_fma_f32 v[60:61], v[10:11], v[62:63], v[60:61] op_sel_hi:[0,1,1]
	v_pk_fma_f32 v[4:5], v[10:11], v[64:65], v[4:5] op_sel_hi:[0,1,1]
	v_pk_fma_f32 v[8:9], v[10:11], v[2:3], v[8:9] op_sel_hi:[0,1,1]
	v_mov_b64_e32 v[0:1], v[164:165]
	v_mov_b64_e32 v[2:3], v[166:167]
	s_nop 0
	v_mov_b32_e32 v10, v174
	s_nop 0
	v_cvt_scalef32_pk_f32_fp4 v[62:63], v0, 1.0
	v_cvt_scalef32_pk_f32_fp4 v[64:65], v0, 1.0 op_sel:[1,0,0]
	v_cvt_scalef32_pk_f32_fp4 v[66:67], v0, 1.0 op_sel:[0,1,0]
	v_cvt_scalef32_pk_f32_fp4 v[68:69], v0, 1.0 op_sel:[1,1,0]
	s_nop 0
	v_pk_fma_f32 v[14:15], v[10:11], v[62:63], v[14:15] op_sel_hi:[0,1,1]
	v_pk_fma_f32 v[16:17], v[10:11], v[64:65], v[16:17] op_sel_hi:[0,1,1]
; __device__ __forceinline__ void row_peer_reduce(const Params& P, unsigned char* ws, int l, int rowi, int lane, float* __restrict__ xout) {
;     ...
; #pragma unroll 4
;     for (int xb_ = 0; xb_ < 8; ++xb_) { const u4 a = *(const u4*)(PARTQ + ((size_t)xb_ * NTOK + ((n + 5u * (unsigned)xb_) & (size_t)(NTOK - 1))) * 1024u + (unsigned)(16 * lane)); const float psc = PSCL[(size_t)xb_ * NTOK + n];
; #pragma unroll
;         for (int d = 0; d < 4; ++d) { const f2 p0 = __builtin_amdgcn_cvt_scalef32_pk_f32_fp4(a[d], 1.0f, 0), p1 = __builtin_amdgcn_cvt_scalef32_pk_f32_fp4(a[d], 1.0f, 1), p2 = __builtin_amdgcn_cvt_scalef32_pk_f32_fp4(a[d], 1.0f, 2), p3 = __builtin_amdgcn_cvt_scalef32_pk_f32_fp4(a[d], 1.0f, 3);
;             const int o = 16 * (d >> 1) + 8 * (d & 1);
;             acc[o] += psc * p0.x; acc[o + 1] += psc * p0.y; acc[o + 2] += psc * p1.x; acc[o + 3] += psc * p1.y; acc[o + 4] += psc * p2.x; acc[o + 5] += psc * p2.y; acc[o + 6] += psc * p3.x; acc[o + 7] += psc * p3.y; } }
;     float s = 0.f;
; #pragma unroll
;     for (int i = 0; i < 32; ++i) s += acc[i];
;     const float mu = wave_sum(s) * (1.f / D); float s2 = 0.f;
	v_pk_fma_f32 v[18:19], v[10:11], v[66:67], v[18:19] op_sel_hi:[0,1,1]
	v_cvt_scalef32_pk_f32_fp4 v[62:63], v1, 1.0
	v_cvt_scalef32_pk_f32_fp4 v[64:65], v1, 1.0 op_sel:[1,0,0]
	v_cvt_scalef32_pk_f32_fp4 v[66:67], v1, 1.0 op_sel:[0,1,0]
	v_cvt_scalef32_pk_f32_fp4 v[0:1], v1, 1.0 op_sel:[1,1,0]
	v_pk_fma_f32 v[6:7], v[10:11], v[0:1], v[6:7] op_sel_hi:[0,1,1]
	v_cvt_scalef32_pk_f32_fp4 v[0:1], v2, 1.0
	v_pk_fma_f32 v[24:25], v[10:11], v[68:69], v[24:25] op_sel_hi:[0,1,1]
	v_pk_fma_f32 v[68:69], v[10:11], v[66:67], v[56:57] op_sel_hi:[0,1,1]
	v_cvt_scalef32_pk_f32_fp4 v[56:57], v2, 1.0 op_sel:[1,0,0]
	v_pk_fma_f32 v[72:73], v[10:11], v[0:1], v[58:59] op_sel_hi:[0,1,1]
	v_cvt_scalef32_pk_f32_fp4 v[0:1], v3, 1.0
	v_pk_fma_f32 v[26:27], v[10:11], v[62:63], v[26:27] op_sel_hi:[0,1,1]
	v_pk_fma_f32 v[30:31], v[10:11], v[64:65], v[30:31] op_sel_hi:[0,1,1]
	v_cvt_scalef32_pk_f32_fp4 v[62:63], v2, 1.0 op_sel:[0,1,0]
	v_cvt_scalef32_pk_f32_fp4 v[64:65], v2, 1.0 op_sel:[1,1,0]
	v_pk_fma_f32 v[28:29], v[10:11], v[56:57], v[28:29] op_sel_hi:[0,1,1]
	v_cvt_scalef32_pk_f32_fp4 v[56:57], v3, 1.0 op_sel:[1,0,0]
	v_cvt_scalef32_pk_f32_fp4 v[58:59], v3, 1.0 op_sel:[0,1,0]
	v_cvt_scalef32_pk_f32_fp4 v[2:3], v3, 1.0 op_sel:[1,1,0]
	v_pk_fma_f32 v[12:13], v[10:11], v[0:1], v[12:13] op_sel_hi:[0,1,1]
	v_pk_fma_f32 v[20:21], v[10:11], v[62:63], v[20:21] op_sel_hi:[0,1,1]
	v_pk_fma_f32 v[22:23], v[10:11], v[64:65], v[22:23] op_sel_hi:[0,1,1]
	v_pk_fma_f32 v[74:75], v[10:11], v[56:57], v[60:61] op_sel_hi:[0,1,1]
	v_pk_fma_f32 v[4:5], v[10:11], v[58:59], v[4:5] op_sel_hi:[0,1,1]
	v_pk_fma_f32 v[8:9], v[10:11], v[2:3], v[8:9] op_sel_hi:[0,1,1]
	v_mov_b64_e32 v[0:1], v[168:169]
	v_mov_b64_e32 v[2:3], v[170:171]
	s_nop 0
	v_mov_b32_e32 v10, v175
	s_nop 0
	v_cvt_scalef32_pk_f32_fp4 v[56:57], v0, 1.0
	v_cvt_scalef32_pk_f32_fp4 v[58:59], v0, 1.0 op_sel:[1,0,0]
	v_cvt_scalef32_pk_f32_fp4 v[60:61], v0, 1.0 op_sel:[0,1,0]
	v_cvt_scalef32_pk_f32_fp4 v[62:63], v0, 1.0 op_sel:[1,1,0]
	s_nop 0
	v_pk_fma_f32 v[56:57], v[10:11], v[56:57], v[14:15] op_sel_hi:[0,1,1]
	v_pk_fma_f32 v[58:59], v[10:11], v[58:59], v[16:17] op_sel_hi:[0,1,1]
	v_pk_fma_f32 v[60:61], v[10:11], v[60:61], v[18:19] op_sel_hi:[0,1,1]
	v_cvt_scalef32_pk_f32_fp4 v[14:15], v1, 1.0
	v_cvt_scalef32_pk_f32_fp4 v[16:17], v1, 1.0 op_sel:[1,0,0]
	v_cvt_scalef32_pk_f32_fp4 v[18:19], v1, 1.0 op_sel:[0,1,0]
	v_cvt_scalef32_pk_f32_fp4 v[0:1], v1, 1.0 op_sel:[1,1,0]
	v_pk_fma_f32 v[64:65], v[10:11], v[14:15], v[26:27] op_sel_hi:[0,1,1]
	v_pk_fma_f32 v[70:71], v[10:11], v[0:1], v[6:7] op_sel_hi:[0,1,1]
	v_cvt_scalef32_pk_f32_fp4 v[0:1], v2, 1.0
	v_cvt_scalef32_pk_f32_fp4 v[6:7], v2, 1.0 op_sel:[1,0,0]
	v_cvt_scalef32_pk_f32_fp4 v[14:15], v2, 1.0 op_sel:[0,1,0]
	v_pk_fma_f32 v[66:67], v[10:11], v[16:17], v[30:31] op_sel_hi:[0,1,1]
	v_cvt_scalef32_pk_f32_fp4 v[16:17], v2, 1.0 op_sel:[1,1,0]
	v_pk_fma_f32 v[72:73], v[10:11], v[0:1], v[72:73] op_sel_hi:[0,1,1]
	v_pk_fma_f32 v[28:29], v[10:11], v[6:7], v[28:29] op_sel_hi:[0,1,1]
	v_pk_fma_f32 v[20:21], v[10:11], v[14:15], v[20:21] op_sel_hi:[0,1,1]
	v_cvt_scalef32_pk_f32_fp4 v[0:1], v3, 1.0
	v_cvt_scalef32_pk_f32_fp4 v[6:7], v3, 1.0 op_sel:[1,0,0]
	v_cvt_scalef32_pk_f32_fp4 v[14:15], v3, 1.0 op_sel:[0,1,0]
	v_cvt_scalef32_pk_f32_fp4 v[2:3], v3, 1.0 op_sel:[1,1,0]
	v_pk_fma_f32 v[62:63], v[10:11], v[62:63], v[24:25] op_sel_hi:[0,1,1]
	v_pk_fma_f32 v[68:69], v[10:11], v[18:19], v[68:69] op_sel_hi:[0,1,1]
	v_pk_fma_f32 v[22:23], v[10:11], v[16:17], v[22:23] op_sel_hi:[0,1,1]
	v_pk_fma_f32 v[12:13], v[10:11], v[0:1], v[12:13] op_sel_hi:[0,1,1]
	v_pk_fma_f32 v[0:1], v[10:11], v[6:7], v[74:75] op_sel_hi:[0,1,1]
	v_pk_fma_f32 v[4:5], v[10:11], v[14:15], v[4:5] op_sel_hi:[0,1,1]
	v_pk_fma_f32 v[2:3], v[10:11], v[2:3], v[8:9] op_sel_hi:[0,1,1]
	s_cbranch_scc0 .LBB0_1593
	v_add_f32_e32 v6, 0, v56
	v_add_f32_e32 v6, v57, v6
	v_add_f32_e32 v6, v58, v6
	v_add_f32_e32 v6, v59, v6
	v_add_f32_e32 v6, v60, v6
	v_add_f32_e32 v6, v61, v6
	v_add_f32_e32 v6, v62, v6
	v_add_f32_e32 v6, v63, v6
	v_add_f32_e32 v6, v64, v6
	v_add_f32_e32 v6, v65, v6
	v_add_f32_e32 v6, v66, v6
	v_add_f32_e32 v6, v67, v6
	v_add_f32_e32 v6, v68, v6
	v_add_f32_e32 v6, v69, v6
	v_add_f32_e32 v6, v70, v6
	v_add_f32_e32 v6, v71, v6
	v_add_f32_e32 v6, v72, v6
	v_add_f32_e32 v6, v73, v6
	v_add_f32_e32 v6, v28, v6
	v_add_f32_e32 v6, v29, v6
	v_add_f32_e32 v6, v20, v6
	v_add_f32_e32 v6, v21, v6
	v_add_f32_e32 v6, v22, v6
	v_add_f32_e32 v6, v23, v6
	v_add_f32_e32 v6, v12, v6
	v_add_f32_e32 v6, v13, v6
	v_add_f32_e32 v6, v0, v6
	v_add_f32_e32 v6, v1, v6
	v_add_f32_e32 v6, v4, v6
	v_add_f32_e32 v6, v5, v6
	v_add_f32_e32 v6, v2, v6
	v_add_f32_e32 v6, v3, v6
	ds_bpermute_b32 v7, v33, v6
	s_lshl_b64 s[4:5], s[6:7], 13
	s_add_u32 s14, s8, s4
	s_addc_u32 s15, s9, s5
	s_waitcnt lgkmcnt(0)
	v_add_f32_e32 v6, v6, v7
	ds_bpermute_b32 v7, v76, v6
	s_waitcnt lgkmcnt(0)
	v_add_f32_e32 v6, v6, v7
	ds_bpermute_b32 v7, v77, v6
	s_waitcnt lgkmcnt(0)
	v_add_f32_e32 v6, v6, v7
	ds_bpermute_b32 v7, v78, v6
	s_waitcnt lgkmcnt(0)
; __device__ __forceinline__ void row_peer_reduce(const Params& P, unsigned char* ws, int l, int rowi, int lane, float* __restrict__ xout) {
;     ...
;     const float mu = wave_sum(s) * (1.f / D); float s2 = 0.f;
; #pragma unroll
;     for (int i = 0; i < 32; ++i) { acc[i] -= mu; s2 += acc[i] * acc[i]; }
;     const float rstd = rsqrtf(wave_sum(s2) * (1.f / D) + LN_EPS);
;     const float* gam = P.in[23] + (size_t)l * D; const float* bet = P.in[24] + (size_t)l * D;
;     bf16* xb = (bf16*)(ws + WS_XB);
; #pragma unroll
;     for (int j = 0; j < 2; ++j) { const int col = 1024 * j + 16 * lane; float o[16];
; #pragma unroll
;         for (int q = 0; q < 4; ++q) { const f4 g4 = *(const f4*)(gam + col + 4 * q), b4 = *(const f4*)(bet + col + 4 * q);
;             o[4 * q] = acc[16 * j + 4 * q] * rstd * g4.x + b4.x; o[4 * q + 1] = acc[16 * j + 4 * q + 1] * rstd * g4.y + b4.y; o[4 * q + 2] = acc[16 * j + 4 * q + 2] * rstd * g4.z + b4.z; o[4 * q + 3] = acc[16 * j + 4 * q + 3] * rstd * g4.w + b4.w;
;             if (xout) *(f4*)(xout + n * D + col + 4 * q) = mk_f4(o[4 * q], o[4 * q + 1], o[4 * q + 2], o[4 * q + 3]); }
	v_add_f32_e32 v6, v6, v7
	v_mov_b32_e32 v7, v6
	s_nop 1
	v_permlane16_swap_b32_e32 v6, v7
	v_add_f32_e32 v6, v6, v7
	v_mov_b32_e32 v7, v6
	s_nop 1
	v_permlane32_swap_b32_e32 v6, v7
	v_add_f32_e32 v6, v6, v7
	v_mul_f32_e32 v74, 0x3a000000, v6
	v_pk_add_f32 v[8:9], v[64:65], v[74:75] op_sel_hi:[1,0] neg_lo:[0,1] neg_hi:[0,1]
	v_pk_add_f32 v[10:11], v[66:67], v[74:75] op_sel_hi:[1,0] neg_lo:[0,1] neg_hi:[0,1]
	v_pk_add_f32 v[26:27], v[22:23], v[74:75] op_sel_hi:[1,0] neg_lo:[0,1] neg_hi:[0,1]
	v_pk_add_f32 v[22:23], v[0:1], v[74:75] op_sel_hi:[1,0] neg_lo:[0,1] neg_hi:[0,1]
	v_pk_add_f32 v[18:19], v[2:3], v[74:75] op_sel_hi:[1,0] neg_lo:[0,1] neg_hi:[0,1]
	global_load_dwordx4 v[0:3], v[44:45], off
	global_load_dwordx4 v[64:67], v[46:47], off
	global_load_dwordx4 v[104:107], v[44:45], off offset:16
	global_load_dwordx4 v[108:111], v[46:47], off offset:16
	global_load_dwordx4 v[112:115], v[44:45], off offset:32
	global_load_dwordx4 v[116:119], v[46:47], off offset:32
	global_load_dwordx4 v[120:123], v[44:45], off offset:48
	global_load_dwordx4 v[124:127], v[46:47], off offset:48
	global_load_dwordx4 v[128:131], v[48:49], off
	global_load_dwordx4 v[132:135], v[50:51], off
	global_load_dwordx4 v[136:139], v[48:49], off offset:16
	global_load_dwordx4 v[140:143], v[50:51], off offset:16
	global_load_dwordx4 v[144:147], v[48:49], off offset:32
	global_load_dwordx4 v[148:151], v[50:51], off offset:32
	global_load_dwordx4 v[152:155], v[48:49], off offset:48
	global_load_dwordx4 v[156:159], v[50:51], off offset:48
	v_pk_add_f32 v[6:7], v[60:61], v[74:75] op_sel_hi:[1,0] neg_lo:[0,1] neg_hi:[0,1]
	v_pk_add_f32 v[62:63], v[62:63], v[74:75] op_sel_hi:[1,0] neg_lo:[0,1] neg_hi:[0,1]
	v_pk_add_f32 v[14:15], v[68:69], v[74:75] op_sel_hi:[1,0] neg_lo:[0,1] neg_hi:[0,1]
	v_pk_add_f32 v[60:61], v[70:71], v[74:75] op_sel_hi:[1,0] neg_lo:[0,1] neg_hi:[0,1]
	v_pk_add_f32 v[30:31], v[72:73], v[74:75] op_sel_hi:[1,0] neg_lo:[0,1] neg_hi:[0,1]
	v_pk_add_f32 v[28:29], v[28:29], v[74:75] op_sel_hi:[1,0] neg_lo:[0,1] neg_hi:[0,1]
	v_pk_add_f32 v[24:25], v[20:21], v[74:75] op_sel_hi:[1,0] neg_lo:[0,1] neg_hi:[0,1]
	v_pk_add_f32 v[20:21], v[12:13], v[74:75] op_sel_hi:[1,0] neg_lo:[0,1] neg_hi:[0,1]
	v_pk_add_f32 v[16:17], v[4:5], v[74:75] op_sel_hi:[1,0] neg_lo:[0,1] neg_hi:[0,1]
	v_pk_add_f32 v[100:101], v[58:59], v[74:75] op_sel_hi:[1,0] neg_lo:[0,1] neg_hi:[0,1]
	v_pk_add_f32 v[74:75], v[56:57], v[74:75] op_sel_hi:[1,0] neg_lo:[0,1] neg_hi:[0,1]
	v_pk_mul_f32 v[58:59], v[100:101], v[100:101]
	v_pk_mul_f32 v[56:57], v[74:75], v[74:75]
	v_pk_mul_f32 v[68:69], v[6:7], v[6:7]
	v_add_f32_e32 v55, v56, v57
	v_add_f32_e32 v55, v58, v55
	v_add_f32_e32 v55, v59, v55
	v_add_f32_e32 v55, v68, v55
	v_pk_mul_f32 v[70:71], v[62:63], v[62:63]
	v_add_f32_e32 v55, v69, v55
	v_add_f32_e32 v55, v70, v55
	v_pk_mul_f32 v[72:73], v[8:9], v[8:9]
	v_add_f32_e32 v55, v71, v55
	v_add_f32_e32 v55, v72, v55
	v_pk_mul_f32 v[82:83], v[10:11], v[10:11]
	v_add_f32_e32 v55, v73, v55
	v_add_f32_e32 v55, v82, v55
	v_pk_mul_f32 v[84:85], v[14:15], v[14:15]
	v_add_f32_e32 v55, v83, v55
	v_add_f32_e32 v55, v84, v55
	v_pk_mul_f32 v[86:87], v[60:61], v[60:61]
	v_add_f32_e32 v55, v85, v55
	v_add_f32_e32 v55, v86, v55
	v_pk_mul_f32 v[88:89], v[30:31], v[30:31]
	v_add_f32_e32 v55, v87, v55
	v_add_f32_e32 v55, v88, v55
	v_pk_mul_f32 v[90:91], v[28:29], v[28:29]
	v_add_f32_e32 v55, v89, v55
	v_add_f32_e32 v55, v90, v55
	v_pk_mul_f32 v[92:93], v[24:25], v[24:25]
	v_add_f32_e32 v55, v91, v55
	v_add_f32_e32 v55, v92, v55
	v_pk_mul_f32 v[94:95], v[26:27], v[26:27]
	v_add_f32_e32 v55, v93, v55
	v_add_f32_e32 v55, v94, v55
	v_pk_mul_f32 v[12:13], v[20:21], v[20:21]
	v_add_f32_e32 v55, v95, v55
	v_add_f32_e32 v12, v12, v55
	v_pk_mul_f32 v[96:97], v[22:23], v[22:23]
	v_add_f32_e32 v12, v13, v12
	v_add_f32_e32 v12, v96, v12
	v_pk_mul_f32 v[4:5], v[16:17], v[16:17]
	v_add_f32_e32 v12, v97, v12
	v_add_f32_e32 v4, v4, v12
	v_pk_mul_f32 v[98:99], v[18:19], v[18:19]
	v_add_f32_e32 v4, v5, v4
	v_add_f32_e32 v4, v98, v4
	v_add_f32_e32 v4, v99, v4
	ds_bpermute_b32 v5, v33, v4
	s_waitcnt lgkmcnt(0)
	v_add_f32_e32 v4, v4, v5
	ds_bpermute_b32 v5, v76, v4
	s_waitcnt lgkmcnt(0)
	v_add_f32_e32 v4, v4, v5
	ds_bpermute_b32 v5, v77, v4
	s_waitcnt lgkmcnt(0)
	v_add_f32_e32 v4, v4, v5
	ds_bpermute_b32 v5, v78, v4
	s_waitcnt lgkmcnt(0)
	v_add_f32_e32 v4, v4, v5
	v_mov_b32_e32 v5, v4
	s_nop 1
	v_permlane16_swap_b32_e32 v4, v5
	v_add_f32_e32 v4, v4, v5
	v_mov_b32_e32 v5, v4
	s_nop 1
	v_permlane32_swap_b32_e32 v4, v5
	v_add_f32_e32 v4, v4, v5
	v_fmamk_f32 v4, v4, 0x3a000000, v194
	v_mul_f32_e32 v5, 0x4b800000, v4
	v_cmp_gt_f32_e32 vcc, s57, v4
	s_nop 1
	v_cndmask_b32_e32 v4, v4, v5, vcc
	v_rsq_f32_e32 v12, v4
	v_lshlrev_b32_e32 v4, 2, v32
	v_mov_b32_e32 v5, v80
	v_lshl_add_u64 v[58:59], s[14:15], 0, v[4:5]
	v_mul_f32_e32 v4, 0x45800000, v12
	v_cndmask_b32_e32 v56, v12, v4, vcc
	v_pk_mul_f32 v[4:5], v[74:75], v[56:57] op_sel_hi:[1,0]
	s_and_b64 vcc, exec, s[10:11]
	s_waitcnt vmcnt(0)
	v_pk_fma_f32 v[0:1], v[0:1], v[4:5], v[64:65]
	v_pk_mul_f32 v[4:5], v[100:101], v[56:57] op_sel_hi:[1,0]
	s_nop 0
	v_pk_fma_f32 v[2:3], v[2:3], v[4:5], v[66:67]
	s_cbranch_vccz .LBB0_1596
	global_store_dwordx4 v[58:59], v[0:3], off
.LBB0_1596:
	s_nop 1
	v_mov_b64_e32 v[64:65], v[104:105]
	v_mov_b64_e32 v[66:67], v[106:107]
	s_nop 1
	v_mov_b64_e32 v[68:69], v[108:109]
	v_mov_b64_e32 v[70:71], v[110:111]
	v_mov_b32_e32 v57, v56
	v_pk_mul_f32 v[4:5], v[6:7], v[56:57]
	v_pk_mul_f32 v[6:7], v[62:63], v[56:57]
	v_cndmask_b32_e64 v12, 0, 1, s[10:11]
	v_cmp_ne_u32_e64 s[4:5], 1, v12
	s_andn2_b64 vcc, exec, s[10:11]
	s_nop 0
	v_pk_fma_f32 v[4:5], v[4:5], v[64:65], v[68:69]
	v_pk_fma_f32 v[6:7], v[6:7], v[66:67], v[70:71]
	s_cbranch_vccnz .LBB0_1598
	global_store_dwordx4 v[58:59], v[4:7], off offset:16
.LBB0_1598:
	s_nop 1
	v_mov_b64_e32 v[62:63], v[112:113]
	v_mov_b64_e32 v[64:65], v[114:115]
	s_nop 1
	v_mov_b64_e32 v[66:67], v[116:117]
	v_mov_b64_e32 v[68:69], v[118:119]
	v_pk_mul_f32 v[8:9], v[8:9], v[56:57]
	v_pk_mul_f32 v[10:11], v[10:11], v[56:57]
	s_and_b64 vcc, exec, s[4:5]
	s_nop 0
	v_pk_fma_f32 v[8:9], v[8:9], v[62:63], v[66:67]
	v_pk_fma_f32 v[10:11], v[10:11], v[64:65], v[68:69]
	s_cbranch_vccnz .LBB0_1600
	global_store_dwordx4 v[58:59], v[8:11], off offset:32
.LBB0_1600:
	s_nop 1
	v_mov_b64_e32 v[62:63], v[120:121]
	v_mov_b64_e32 v[64:65], v[122:123]
	s_nop 1
	v_mov_b64_e32 v[66:67], v[124:125]
	v_mov_b64_e32 v[68:69], v[126:127]
	s_add_u32 s12, s36, s12
	v_pk_mul_f32 v[12:13], v[14:15], v[56:57]
	v_pk_mul_f32 v[14:15], v[60:61], v[56:57]
	v_readlane_b32 s28, v254, 35
	s_addc_u32 s13, s40, s13
	s_and_b64 vcc, exec, s[4:5]
	v_readlane_b32 s18, v254, 50
	v_readlane_b32 s29, v254, 36
	v_readlane_b32 s19, v254, 51
	s_nop 0
	v_pk_fma_f32 v[12:13], v[12:13], v[62:63], v[66:67]
	v_pk_fma_f32 v[14:15], v[14:15], v[64:65], v[68:69]
	s_cbranch_vccnz .LBB0_1611
	global_store_dwordx4 v[58:59], v[12:15], off offset:48
	v_lshlrev_b32_e32 v58, 1, v32
	s_cbranch_execnz .LBB0_1603

; __device__ __forceinline__ void row_peer_reduce(const Params& P, unsigned char* ws, int l, int rowi, int lane, float* __restrict__ xout) {
;     ...
;     for (int j = 0; j < 2; ++j) { const int col = 1024 * j + 16 * lane; float o[16];
; #pragma unroll
;         for (int q = 0; q < 4; ++q) { const f4 g4 = *(const f4*)(gam + col + 4 * q), b4 = *(const f4*)(bet + col + 4 * q);
;             o[4 * q] = acc[16 * j + 4 * q] * rstd * g4.x + b4.x; o[4 * q + 1] = acc[16 * j + 4 * q + 1] * rstd * g4.y + b4.y; o[4 * q + 2] = acc[16 * j + 4 * q + 2] * rstd * g4.z + b4.z; o[4 * q + 3] = acc[16 * j + 4 * q + 3] * rstd * g4.w + b4.w;
;             if (xout) *(f4*)(xout + n * D + col + 4 * q) = mk_f4(o[4 * q], o[4 * q + 1], o[4 * q + 2], o[4 * q + 3]); }
.LBB0_1603:
	s_nop 1
	v_mov_b64_e32 v[0:1], v[128:129]
	v_mov_b64_e32 v[2:3], v[130:131]
	s_nop 0
	s_nop 1
	v_mov_b64_e32 v[4:5], v[132:133]
	v_mov_b64_e32 v[6:7], v[134:135]
	v_mov_b32_e32 v55, v80
	v_pk_mul_f32 v[8:9], v[30:31], v[56:57]
	v_pk_mul_f32 v[10:11], v[28:29], v[56:57]
	s_and_b64 vcc, exec, s[4:5]
	v_lshl_add_u64 v[28:29], s[14:15], 0, v[54:55]
	s_nop 0
	v_pk_fma_f32 v[0:1], v[8:9], v[0:1], v[4:5]
	v_pk_fma_f32 v[2:3], v[10:11], v[2:3], v[6:7]
	s_cbranch_vccnz .LBB0_1605
	global_store_dwordx4 v[28:29], v[0:3], off
.LBB0_1605:
	s_nop 1
	v_mov_b64_e32 v[4:5], v[136:137]
	v_mov_b64_e32 v[6:7], v[138:139]
	s_nop 1
	v_mov_b64_e32 v[8:9], v[140:141]
	v_mov_b64_e32 v[10:11], v[142:143]
	v_pk_mul_f32 v[12:13], v[24:25], v[56:57]
	v_pk_mul_f32 v[14:15], v[26:27], v[56:57]
	s_and_b64 vcc, exec, s[4:5]
	s_nop 0
	v_pk_fma_f32 v[4:5], v[12:13], v[4:5], v[8:9]
	v_pk_fma_f32 v[6:7], v[14:15], v[6:7], v[10:11]
	s_cbranch_vccnz .LBB0_1607
	global_store_dwordx4 v[28:29], v[4:7], off offset:16
.LBB0_1607:
	s_nop 1
	v_mov_b64_e32 v[8:9], v[144:145]
	v_mov_b64_e32 v[10:11], v[146:147]
	s_nop 1
	v_mov_b64_e32 v[12:13], v[148:149]
	v_mov_b64_e32 v[14:15], v[150:151]
	v_pk_mul_f32 v[20:21], v[20:21], v[56:57]
	v_pk_mul_f32 v[22:23], v[22:23], v[56:57]
	s_and_b64 vcc, exec, s[4:5]
	s_nop 0
	v_pk_fma_f32 v[8:9], v[20:21], v[8:9], v[12:13]
	v_pk_fma_f32 v[10:11], v[22:23], v[10:11], v[14:15]
	s_cbranch_vccnz .LBB0_1609
	global_store_dwordx4 v[28:29], v[8:11], off offset:32
.LBB0_1609:
	s_nop 1
	v_mov_b64_e32 v[12:13], v[152:153]
	v_mov_b64_e32 v[14:15], v[154:155]
	s_nop 1
	v_mov_b64_e32 v[20:21], v[156:157]
	v_mov_b64_e32 v[22:23], v[158:159]
	v_pk_mul_f32 v[16:17], v[16:17], v[56:57]
	v_pk_mul_f32 v[18:19], v[18:19], v[56:57]
	s_and_b64 vcc, exec, s[4:5]
	s_nop 0
	v_pk_fma_f32 v[12:13], v[16:17], v[12:13], v[20:21]
	v_pk_fma_f32 v[14:15], v[18:19], v[14:15], v[22:23]
	s_cbranch_vccnz .LBB0_1612
	global_store_dwordx4 v[28:29], v[12:15], off offset:48
	s_cbranch_execnz .LBB0_1591
	s_branch .LBB0_1590
